# conversion-first workgroups are the first 12 of each XCD's 32 (contiguous) instead of 3 of every 8
# baseline (speedup 1.0000x reference)
; #define LAS __attribute__((address_space(3)))
; #define RUN(k, ...) do { __VA_ARGS__; } while (0)
; __device__ __forceinline__ void attn_queues(const P& p, LAS unsigned char* lds, int* ctr, const int xg) {
;     LAS int* qs = (LAS int*)(lds + LDS_FLAG + 64);
;     const int tid = threadIdx.x, nq = xg >= 0 ? 4 * 16 : NB * 8 * 16;
;     int* c0 = ctr + (xg >= 0 ? xg : 0); int* c1 = ctr + 64 + (xg >= 0 ? xg : 0);
;     {   if (tid == 0) qs[0] = atomicAdd(c0, 1);
; __device__ __forceinline__ void phase_attn(const P& p, LAS unsigned char* lds, int G, int bid) {
;     int* ctr = (int*)(p.ws + WS_CTL + 61440); const int xg = (G == 256) ? (bid & 7) : -1;
;     if (MOE_FP8 && ((bid >> 3) & 7) < 3) { conv_queue(p, lds, ctr + 128, -1); attn_queues(p, lds, ctr, xg); }
;     else { attn_queues(p, lds, ctr, xg); if (MOE_FP8) conv_queue(p, lds, ctr + 128, -1); }
; __global__ void __launch_bounds__(512, 2) mega(P p, int lo, int hi, int bar_idx) {
;     ...
;     if (IN(4)) RUN(4, at::phase_attn(p, lds, G, bid));
.LBB0_688:
	s_cmp_lt_i32 s88, 5
	s_cselect_b64 s[2:3], -1, 0
	s_and_b64 s[0:1], s[2:3], s[0:1]
	s_andn2_b64 vcc, exec, s[0:1]
	v_writelane_b32 v242, s76, 35
	s_cbranch_vccnz .LBB0_924
	s_add_u32 s0, s74, 0xf000
	v_writelane_b32 v242, s0, 36
	s_addc_u32 s0, s75, 0
	s_cmpk_lg_i32 s76, 0x100
	v_writelane_b32 v242, s0, 37
	s_cselect_b64 s[0:1], -1, 0
	s_and_b32 s4, s70, 7
	v_writelane_b32 v242, s0, 38
	s_cmpk_eq_i32 s76, 0x100
	s_nop 0
	v_writelane_b32 v242, s1, 39
	s_cselect_b64 s[0:1], -1, 0
	v_writelane_b32 v242, s0, 40
	s_nop 1
	v_writelane_b32 v242, s1, 41
	s_and_b64 s[0:1], s[0:1], exec
	v_writelane_b32 v242, s4, 42
	s_cselect_b32 s0, s4, -1
	v_writelane_b32 v242, s0, 43
	s_lshr_b32 s0, s70, 3
	s_cmp_gt_u32 s0, 11
	s_mov_b64 s[0:1], -1
	v_writelane_b32 v242, s2, 44
	s_nop 1
	v_writelane_b32 v242, s3, 45
	s_cbranch_scc0 .LBB0_806
	v_readlane_b32 s0, v242, 40
	v_readlane_b32 s1, v242, 41
	s_and_b64 s[0:1], s[0:1], exec
	v_readlane_b32 s0, v242, 42
	s_cselect_b32 s0, s0, 0
	s_lshl_b32 s33, s0, 2
	v_readlane_b32 s0, v242, 36
	s_add_u32 s70, s0, s33
	v_readlane_b32 s0, v242, 37
	s_addc_u32 s71, s0, 0
	s_mov_b64 s[0:1], exec
	v_readlane_b32 s2, v242, 31
	v_readlane_b32 s3, v242, 32
	s_and_b64 s[2:3], s[0:1], s[2:3]
	s_mov_b64 exec, s[2:3]
	s_cbranch_execz .LBB0_694
	s_mov_b64 s[6:7], exec
	v_mbcnt_lo_u32_b32 v1, s6, 0
	v_mbcnt_hi_u32_b32 v1, s7, v1
	v_cmp_eq_u32_e32 vcc, 0, v1
	s_and_saveexec_b64 s[4:5], vcc
	s_cbranch_execz .LBB0_693
	s_bcnt1_i32_b64 s2, s[6:7]
	s_waitcnt vmcnt(3)
	v_mov_b32_e32 v2, 0
	v_mov_b32_e32 v3, s2
	global_atomic_add v2, v2, v3, s[70:71] sc0
